# v15 + diff loop copy 1 also de-bursts (waves 4-7 issue K/V DMA after 4th QK MFMA with their own tile-base select)
# speedup vs baseline: 1.0206x; 1.0024x over previous
; #define DMA_WAIT(last) do { if (last) asm volatile("s_waitcnt vmcnt(0)" ::: "memory"); else asm volatile("s_waitcnt vmcnt(%0)" :: "n"(NPW) : "memory"); } while (0)
; template <int DK, int DV, bool OFF, class QLoader> ...
;     ...
;   f32x16 pA0, pA1, pB0, pB1; bf16x8 pa0, pa1, pa2, pa3; const int NT = nkeys / KVBLK;
;   DMA_TILE(0, 0); DMA_TILE(1, 1); DMA_WAIT(false); __syncthreads(); if (2 < NT) DMA_TILE(2, 2);
;   qkt<DK>(pA0, pA1, K_lds, qr, r32, hi); partialSM<DK, OFF>(pA0, pA1, negMC);
.LBB0_844:
.LBB0_846:
	s_add_i32 s28, s55, -3
	s_cmp_lt_u32 s28, s95
	s_cselect_b64 s[24:25], -1, 0
	s_cmp_ge_u32 s28, s95
	s_cselect_b64 s[28:29], -1, 0
	s_and_b64 vcc, exec, s[28:29]
	s_waitcnt vmcnt(0)
	s_barrier
	s_cbranch_vccnz .LBB0_856
	s_cmp_lg_u32 s80, 0
	s_cbranch_scc1 .LBB0_856
	s_cmp_gt_u32 s57, 1
	s_cselect_b64 s[36:37], -1, 0
	s_mov_b64 s[38:39], -1
	s_and_b64 vcc, exec, s[36:37]
	s_cbranch_vccz .LBB0_851
	s_lshl_b64 s[30:31], s[2:3], 7
	s_add_u32 s30, s93, s30
	s_addc_u32 s31, s94, s31
	s_cbranch_execz .LBB0_852

; template <int DK>
; __device__ __forceinline__ void qkt(f32x16& p0, f32x16& p1, const char* Ks, const bf16x8* qr, int r32, int hi) {
;   p0 = f32x16{}; p1 = f32x16{};
; #pragma unroll
;   for (int d0 = 0; d0 < DK / 16; ++d0) { const int cb = (d0 * 16 + hi * 8) * 2;
;     const bf16x8 b0 = *reinterpret_cast<const bf16x8*>(Ks + ATT_KSWZ(r32, cb));
;     const bf16x8 b1 = *reinterpret_cast<const bf16x8*>(Ks + ATT_KSWZ(32 + r32, cb));
;     p0 = __builtin_amdgcn_mfma_f32_32x32x16_bf16(b0, qr[d0], p0, 0, 0, 0);
;     p1 = __builtin_amdgcn_mfma_f32_32x32x16_bf16(b1, qr[d0], p1, 0, 0, 0);
;   }
; }
.LBB0_856:
	ds_read_b128 v[82:85], v162 offset:16384
	ds_read_b128 v[86:89], v162 offset:20480
	ds_read_b128 v[130:133], v164 offset:16384
	ds_read_b128 v[134:137], v164 offset:20480
	v_exp_f32_e32 v66, v66
	v_add_f32_e32 v180, 0, v173
	v_add_f32_e32 v180, v174, v180
	v_add_f32_e32 v180, v175, v180
	v_add_f32_e32 v180, v184, v180
	v_add_f32_e32 v180, v185, v180
	v_add_f32_e32 v180, v186, v180
	v_add_f32_e32 v180, v187, v180
	v_add_f32_e32 v180, v188, v180
	v_add_f32_e32 v180, v189, v180
	v_add_f32_e32 v180, v190, v180
	v_add_f32_e32 v180, v191, v180
	v_add_f32_e32 v180, v192, v180
	v_add_f32_e32 v180, v193, v180
	v_add_f32_e32 v180, v194, v180
	v_add_f32_e32 v180, v195, v180
	v_add_f32_e32 v180, v196, v180
	s_waitcnt lgkmcnt(0)
	v_mfma_f32_32x32x16_bf16 v[98:113], v[82:85], v[114:117], 0
	v_exp_f32_e32 v67, v67
	v_exp_f32_e32 v68, v68
	v_exp_f32_e32 v69, v69
	v_exp_f32_e32 v70, v70
	v_exp_f32_e32 v71, v71
	v_exp_f32_e32 v72, v72
	v_exp_f32_e32 v73, v73
	v_mfma_f32_32x32x16_bf16 v[82:97], v[86:89], v[114:117], 0
	v_exp_f32_e32 v74, v74
	v_exp_f32_e32 v75, v75
	v_exp_f32_e32 v76, v76
	v_exp_f32_e32 v77, v77
	v_exp_f32_e32 v78, v78
	v_exp_f32_e32 v79, v79
	v_exp_f32_e32 v80, v80
	v_mfma_f32_32x32x16_bf16 v[98:113], v[130:133], v[118:121], v[98:113]
	v_exp_f32_e32 v81, v81
	s_andn2_b64 vcc, exec, s[26:27]
	v_mfma_f32_32x32x16_bf16 v[82:97], v[134:137], v[118:121], v[82:97]
	s_cmp_eq_u32 s80, 0
	s_cbranch_scc1 .Lstg_c1_done
	s_add_i32 s32, s55, -3
	s_cmp_ge_u32 s32, s95
	s_cbranch_scc1 .Lstg_c1_done
	s_add_i32 s32, s55, -5
	s_cmp_gt_u32 s32, 1
	s_cbranch_scc0 .Lstg_c1_ctx
	s_lshl_b64 s[30:31], s[2:3], 7
	s_add_u32 s30, s93, s30
	s_addc_u32 s31, s94, s31
	s_mul_i32 s36, s2, 0x1800
	s_mul_hi_u32 s37, s2, 0x1800
	s_add_u32 s36, s74, s36
	s_addc_u32 s37, s75, s37
	s_branch .Lstg_c1_issue
.Lstg_c1_ctx:
	s_add_u32 s30, s60, s8
	s_addc_u32 s31, s45, s9
	s_add_u32 s36, s4, s8
	s_addc_u32 s37, s5, s9

; __device__ __forceinline__ void finishSM(f32x16& p0, f32x16& p1, float& l_reg, bf16x8& pa0, bf16x8& pa1, bf16x8& pa2, bf16x8& pa3) {
; #pragma unroll
;   for (int r = 0; r < 16; ++r) p1[r] = __builtin_amdgcn_exp2f(p1[r]);
;   float ps = 0;
; #pragma unroll
;   for (int r = 0; r < 16; ++r) ps += p0[r];
; #pragma unroll
;   for (int r = 0; r < 16; ++r) ps += p1[r];
;   l_reg += ps;
;     ...
;   ATT_PK4(p0, 0, pa0); ATT_PK4(p0, 8, pa1); ATT_PK4(p1, 0, pa2); ATT_PK4(p1, 8, pa3);
;     ...
; }
; template <int DK>
; __device__ __forceinline__ void qkt(f32x16& p0, f32x16& p1, const char* Ks, const bf16x8* qr, int r32, int hi) {
;   p0 = f32x16{}; p1 = f32x16{};
; #pragma unroll
;   for (int d0 = 0; d0 < DK / 16; ++d0) { const int cb = (d0 * 16 + hi * 8) * 2;
;     const bf16x8 b0 = *reinterpret_cast<const bf16x8*>(Ks + ATT_KSWZ(r32, cb));
;     const bf16x8 b1 = *reinterpret_cast<const bf16x8*>(Ks + ATT_KSWZ(32 + r32, cb));
;     p0 = __builtin_amdgcn_mfma_f32_32x32x16_bf16(b0, qr[d0], p0, 0, 0, 0);
;     p1 = __builtin_amdgcn_mfma_f32_32x32x16_bf16(b1, qr[d0], p1, 0, 0, 0);
;   }
; }
; template <int DV, int GRP> __device__ __forceinline__ void v_group_read(s16x4* vf, int vb) {
;   sfor<0, 8>([&](auto ic) { constexpr int j = decltype(ic)::value; vf[j] = tr_read<v_rd_off<DV>(GRP, j / 2, j % 2)>(vb); });
; }
; __device__ __forceinline__ void pv_group(f32x16& od, const s16x4* vf, bf16x8 pa0, bf16x8 pa1, bf16x8 pa2, bf16x8 pa3) {
;     ...
;   od = __builtin_amdgcn_mfma_f32_32x32x16_bf16(pa0, ATT_PK(vf[0], vf[1]), od, 0, 0, 0);
;   od = __builtin_amdgcn_mfma_f32_32x32x16_bf16(pa1, ATT_PK(vf[2], vf[3]), od, 0, 0, 0);
;   od = __builtin_amdgcn_mfma_f32_32x32x16_bf16(pa2, ATT_PK(vf[4], vf[5]), od, 0, 0, 0);
;   od = __builtin_amdgcn_mfma_f32_32x32x16_bf16(pa3, ATT_PK(vf[6], vf[7]), od, 0, 0, 0);
;     ...
; }
; template <int DV> __device__ __forceinline__ void pv_all_pipe(f32x16* o, int vb, bf16x8 pa0, bf16x8 pa1, bf16x8 pa2, bf16x8 pa3) {
;   s16x4 va[8], vc[8];
;   v_group_read<DV, 0>(va, vb); v_group_read<DV, 1>(vc, vb);
;   lgkm_wait8<8>(va); pv_group(o[0], va, pa0, pa1, pa2, pa3);
;   if constexpr (DV == 128) {
;     s16x4 vd[8], ve[8];
;     v_group_read<DV, 2>(vd, vb);
;     lgkm_wait8<8>(vc); pv_group(o[1], vc, pa0, pa1, pa2, pa3);
;     v_group_read<DV, 3>(ve, vb);
;     lgkm_wait8<8>(vd); pv_group(o[2], vd, pa0, pa1, pa2, pa3);
;     lgkm_wait8<0>(ve); pv_group(o[3], ve, pa0, pa1, pa2, pa3);
.Lstg_c1_done:
	ds_read_b128 v[130:133], v166 offset:16384
	ds_read_b128 v[134:137], v166 offset:20480
	v_add_f32_e32 v180, v66, v180
	v_add_f32_e32 v180, v67, v180
	v_add_f32_e32 v180, v68, v180
	v_add_f32_e32 v180, v69, v180
	v_add_f32_e32 v180, v70, v180
	v_add_f32_e32 v180, v71, v180
	v_add_f32_e32 v180, v72, v180
	v_add_f32_e32 v180, v73, v180
	s_waitcnt lgkmcnt(0)
	v_mfma_f32_32x32x16_bf16 v[98:113], v[130:133], v[122:125], v[98:113]
	v_mfma_f32_32x32x16_bf16 v[82:97], v[134:137], v[122:125], v[82:97]
	ds_read_b128 v[130:133], v168 offset:16384
	ds_read_b128 v[134:137], v168 offset:20480
	v_add_f32_e32 v180, v74, v180
	v_add_f32_e32 v180, v75, v180
	v_add_f32_e32 v180, v76, v180
	v_add_f32_e32 v180, v77, v180
	v_add_f32_e32 v180, v78, v180
	v_add_f32_e32 v180, v79, v180
	v_add_f32_e32 v180, v80, v180
	v_add_f32_e32 v180, v81, v180
	s_waitcnt lgkmcnt(0)
	v_mfma_f32_32x32x16_bf16 v[98:113], v[130:133], v[126:129], v[98:113]
	v_mfma_f32_32x32x16_bf16 v[82:97], v[134:137], v[126:129], v[82:97]
	v_add_f32_e32 v172, v172, v180
	v_cvt_pk_bf16_f32 v130, v173, v174
	v_cvt_pk_bf16_f32 v131, v175, v184
	v_cvt_pk_bf16_f32 v132, v185, v186
	v_cvt_pk_bf16_f32 v133, v187, v188
	v_cvt_pk_bf16_f32 v134, v189, v190
	v_cvt_pk_bf16_f32 v135, v191, v192
	v_cvt_pk_bf16_f32 v136, v193, v194
	v_cvt_pk_bf16_f32 v137, v195, v196
	v_cvt_pk_bf16_f32 v138, v66, v67
	v_cvt_pk_bf16_f32 v139, v68, v69
	v_cvt_pk_bf16_f32 v140, v70, v71
	v_cvt_pk_bf16_f32 v141, v72, v73
	v_cvt_pk_bf16_f32 v142, v74, v75
	v_cvt_pk_bf16_f32 v143, v76, v77
	v_cvt_pk_bf16_f32 v144, v78, v79
	v_cvt_pk_bf16_f32 v145, v80, v81
	ds_read_b64_tr_b16 v[176:177], v169 offset:0
	ds_read_b64_tr_b16 v[178:179], v169 offset:0x800
	ds_read_b64_tr_b16 v[198:199], v169 offset:0x1000
	ds_read_b64_tr_b16 v[200:201], v169 offset:0x1800
	ds_read_b64_tr_b16 v[202:203], v169 offset:0x2000
	ds_read_b64_tr_b16 v[204:205], v169 offset:0x2800
	ds_read_b64_tr_b16 v[206:207], v169 offset:0x3000
	ds_read_b64_tr_b16 v[208:209], v169 offset:0x3800
	ds_read_b64_tr_b16 v[210:211], v169 offset:0x200
	ds_read_b64_tr_b16 v[212:213], v169 offset:0xa00
	ds_read_b64_tr_b16 v[214:215], v169 offset:0x1200
	s_nop 0
	v_permlane32_swap_b32_e32 v130, v132
	v_permlane32_swap_b32_e32 v131, v133
	ds_read_b64_tr_b16 v[216:217], v169 offset:0x1a00
	ds_read_b64_tr_b16 v[218:219], v169 offset:0x2200
	ds_read_b64_tr_b16 v[220:221], v169 offset:0x2a00
	ds_read_b64_tr_b16 v[222:223], v169 offset:0x3200
	ds_read_b64_tr_b16 v[224:225], v169 offset:0x3a00
	s_waitcnt lgkmcnt(8)
	v_permlane32_swap_b32_e32 v134, v136
	s_nop 0
	v_mfma_f32_32x32x16_bf16 v[2:17], v[130:133], v[176:179], v[2:17]
	v_permlane32_swap_b32_e32 v135, v137
	v_permlane32_swap_b32_e32 v138, v140
	v_permlane32_swap_b32_e32 v139, v141
	ds_read_b64_tr_b16 v[176:177], v169 offset:0x400
	v_mfma_f32_32x32x16_bf16 v[2:17], v[134:137], v[198:201], v[2:17]
	v_permlane32_swap_b32_e32 v142, v144
	v_permlane32_swap_b32_e32 v143, v145
	ds_read_b64_tr_b16 v[178:179], v169 offset:0xc00
	ds_read_b64_tr_b16 v[198:199], v169 offset:0x1400
	ds_read_b64_tr_b16 v[200:201], v169 offset:0x1c00
	v_mfma_f32_32x32x16_bf16 v[2:17], v[138:141], v[202:205], v[2:17]
	ds_read_b64_tr_b16 v[202:203], v169 offset:0x2400
	ds_read_b64_tr_b16 v[204:205], v169 offset:0x2c00
	v_exp_f32_e32 v197, v98
	v_mfma_f32_32x32x16_bf16 v[2:17], v[142:145], v[206:209], v[2:17]
	ds_read_b64_tr_b16 v[206:207], v169 offset:0x3400
	ds_read_b64_tr_b16 v[208:209], v169 offset:0x3c00
	s_waitcnt lgkmcnt(8)
	s_nop 0
	v_mfma_f32_32x32x16_bf16 v[50:65], v[130:133], v[210:213], v[50:65]
	ds_read_b64_tr_b16 v[210:211], v169 offset:0x600
	ds_read_b64_tr_b16 v[212:213], v169 offset:0xe00
	v_mfma_f32_32x32x16_bf16 v[50:65], v[134:137], v[214:217], v[50:65]
	ds_read_b64_tr_b16 v[214:215], v169 offset:0x1600
	ds_read_b64_tr_b16 v[216:217], v169 offset:0x1e00
	v_mfma_f32_32x32x16_bf16 v[50:65], v[138:141], v[218:221], v[50:65]
	ds_read_b64_tr_b16 v[218:219], v169 offset:0x2600
	ds_read_b64_tr_b16 v[220:221], v169 offset:0x2e00
	v_mfma_f32_32x32x16_bf16 v[50:65], v[142:145], v[222:225], v[50:65]
	ds_read_b64_tr_b16 v[222:223], v169 offset:0x3600
	ds_read_b64_tr_b16 v[224:225], v169 offset:0x3e00
	s_waitcnt lgkmcnt(8)
	s_nop 0
	s_waitcnt lgkmcnt(0)
	v_mfma_f32_32x32x16_bf16 v[34:49], v[130:133], v[176:179], v[34:49]
	v_mfma_f32_32x32x16_bf16 v[18:33], v[130:133], v[210:213], v[18:33]
	v_exp_f32_e32 v210, v105
	v_exp_f32_e32 v211, v111
	v_exp_f32_e32 v212, v113
	v_mfma_f32_32x32x16_bf16 v[34:49], v[134:137], v[198:201], v[34:49]
	v_exp_f32_e32 v200, v99
	v_exp_f32_e32 v198, v100
	v_exp_f32_e32 v199, v106
	v_exp_f32_e32 v201, v108
	v_mfma_f32_32x32x16_bf16 v[18:33], v[134:137], v[214:217], v[18:33]
	v_mfma_f32_32x32x16_bf16 v[34:49], v[138:141], v[202:205], v[34:49]
	v_exp_f32_e32 v202, v101
	v_exp_f32_e32 v204, v102
	v_exp_f32_e32 v205, v104
	v_exp_f32_e32 v203, v107
	v_mfma_f32_32x32x16_bf16 v[18:33], v[138:141], v[218:221], v[18:33]
	v_mfma_f32_32x32x16_bf16 v[34:49], v[142:145], v[206:209], v[34:49]
	v_exp_f32_e32 v207, v103
	v_exp_f32_e32 v209, v109
	v_exp_f32_e32 v206, v110
	v_exp_f32_e32 v208, v112
	v_mfma_f32_32x32x16_bf16 v[18:33], v[142:145], v[222:225], v[18:33]
	s_cbranch_vccnz .LBB0_865
